# work-queue: next unit index prefetched at the top of dynamic units (not the static first unit) in stages A and C; GEMM prio trims
# baseline (speedup 1.0000x reference)
.LBB0_380:
	s_mov_b32 s101, 0
	s_cmpk_lt_u32 s26, 0x100
	s_cbranch_scc1 .Lwqa_nopf
	s_mov_b32 s101, 1
	v_readfirstlane_b32 s100, v0
	s_cmp_lt_u32 s100, 64
	s_cbranch_scc0 .Lwqa_skip
	s_mov_b64 exec, 1
	v_add_u32_e32 v255, s76, v211
	global_atomic_add v255, v255, v208, s[36:37] sc0
	s_mov_b64 exec, -1
.Lwqa_skip:
.Lwqa_nopf:
	s_mov_b32 s30, 0
	v_mov_b32_e32 v168, v0
	s_cmpk_gt_i32 s26, 0x9f
	s_cbranch_scc0 .LBB0_448
	s_cmpk_gt_u32 s26, 0x11f
	s_cbranch_scc0 .LBB0_449
	s_cmpk_gt_u32 s26, 0x21f
	s_cbranch_scc0 .LBB0_450
	s_cmpk_gt_u32 s26, 0x29f
	s_cbranch_scc0 .LBB0_451
	s_cmpk_gt_u32 s26, 0x39f
	s_cbranch_scc0 .LBB0_452
	s_cmpk_gt_u32 s26, 0x59f
	s_cbranch_scc0 .LBB0_453
	s_cmpk_lt_u32 s26, 0x8e8
	v_readlane_b32 s4, v253, 45
	s_cselect_b64 s[0:1], -1, 0
	v_readlane_b32 s5, v253, 46
	s_and_b64 s[4:5], s[4:5], s[0:1]
	s_mov_b64 s[0:1], 0
	s_and_b64 vcc, exec, s[4:5]
	s_mov_b64 s[4:5], 0
	s_cbranch_vccz .LBB0_454
	s_ashr_i32 s31, s30, 31
	s_lshl_b64 s[6:7], s[30:31], 2
	s_add_u32 s4, s93, s6
	v_readlane_b32 s5, v253, 32
	s_addc_u32 s5, s5, s7
	s_lshl_b32 s10, s26, 1
	s_add_i32 s8, s10, 0xf4c0
	s_and_b32 s9, s8, 0xfffe
	s_mulk_i32 s9, 0x4e05
	s_lshr_b32 s11, s9, 21
	s_mulk_i32 s11, 0x69
	s_sub_i32 s8, s8, s11
	s_lshr_b32 s9, s9, 14
	s_lshl_b32 s8, s8, 7
	v_lshlrev_b32_e32 v1, 2, v168
	s_and_b32 s78, s9, 0xff80
	s_and_b32 s21, s8, 0xff80
	v_and_b32_e32 v14, 0x7c, v1
	v_ashrrev_i32_e32 v68, 5, v168
	s_waitcnt lgkmcnt(0)
	v_or_b32_e32 v2, s21, v14
	s_movk_i32 s8, 0x3410
	v_add_u32_e32 v10, s78, v68
	v_readfirstlane_b32 s13, v168
	v_cmp_gt_u32_e32 vcc, s8, v2
	v_ashrrev_i32_e32 v11, 31, v10
	v_mov_b32_e32 v8, 0
	v_lshlrev_b32_e32 v2, 2, v2
	v_mov_b32_e32 v4, 0
	v_mov_b32_e32 v5, 0
	v_mov_b32_e32 v6, 0
	v_mov_b32_e32 v7, 0
	s_and_saveexec_b64 s[8:9], vcc
	s_cbranch_execz .LBB0_389
	v_mov_b64_e32 v[4:5], s[4:5]
	s_mov_b32 s11, 0xd040
	v_mad_i64_i32 v[4:5], s[22:23], v10, s11, v[4:5]
	v_lshl_add_u64 v[4:5], v[4:5], 0, v[2:3]
	global_load_dwordx4 v[4:7], v[4:5], off

.LBB0_726:
	s_mov_b64 s[0:1], -1
	s_and_b64 vcc, exec, s[4:5]
	s_cbranch_vccz .LBB0_379
	v_cmp_eq_u32_e32 vcc, 0, v168
	s_waitcnt vmcnt(0) lgkmcnt(0)
	s_barrier
	s_and_saveexec_b64 s[0:1], vcc
	s_cbranch_execz .LBB0_378
	s_mov_b64 s[6:7], exec
	v_mbcnt_lo_u32_b32 v1, s6, 0
	v_mbcnt_hi_u32_b32 v1, s7, v1
	v_cmp_eq_u32_e32 vcc, 0, v1
	s_and_saveexec_b64 s[4:5], vcc
	s_cbranch_execz .LBB0_377
	s_cmp_eq_u32 s101, 0
	s_cbranch_scc1 .Lwqa_blk
	v_mov_b32_e32 v2, v255
	s_branch .LBB0_377
.Lwqa_blk:
	s_ashr_i32 s8, s30, 31
	s_add_u32 s9, s36, s30
	s_addc_u32 s10, s37, s8
	s_add_u32 s8, s9, s76
	s_addc_u32 s9, s10, s77
	s_bcnt1_i32_b64 s6, s[6:7]
	v_mov_b32_e32 v2, s6
	global_atomic_add v2, v211, v2, s[8:9] sc0
	s_branch .LBB0_377

.LBB0_851:
	s_mov_b32 s101, 0
	s_cmpk_lt_u32 s26, 0x100
	s_cbranch_scc1 .Lwqc_nopf
	v_readfirstlane_b32 s100, v0
	s_cmp_lt_u32 s100, 64
	s_cbranch_scc0 .Lwqc_skip
	s_mov_b64 exec, 1
	v_readlane_b32 s100, v253, 43
	v_readlane_b32 s101, v253, 44
	v_mov_b32_e32 v255, v211
	s_nop 4
	global_atomic_add v255, v255, v208, s[100:101] offset:256 sc0
	s_mov_b64 exec, -1
.Lwqc_skip:
	s_mov_b32 s101, 1

.LBB0_1132:
	s_mov_b64 s[0:1], -1
	s_and_b64 vcc, exec, s[4:5]
	s_cbranch_vccz .LBB0_850
	v_cmp_eq_u32_e32 vcc, 0, v204
	s_waitcnt vmcnt(0) lgkmcnt(0)
	s_barrier
	s_and_saveexec_b64 s[0:1], vcc
	s_cbranch_execz .LBB0_849
	s_mov_b64 s[6:7], exec
	v_mbcnt_lo_u32_b32 v1, s6, 0
	v_mbcnt_hi_u32_b32 v1, s7, v1
	v_cmp_eq_u32_e32 vcc, 0, v1
	s_and_saveexec_b64 s[4:5], vcc
	s_cbranch_execz .LBB0_848
	s_cmp_eq_u32 s101, 0
	s_cbranch_scc1 .Lwqc_blk
	v_mov_b32_e32 v2, v255
	s_branch .LBB0_848
.Lwqc_blk:
	s_ashr_i32 s9, s74, 31
	v_readlane_b32 s8, v253, 43
	s_add_u32 s8, s8, s74
	v_readlane_b32 s10, v253, 44
	s_addc_u32 s9, s10, s9
	s_bcnt1_i32_b64 s6, s[6:7]
	v_mov_b32_e32 v2, s6
	global_atomic_add v2, v211, v2, s[8:9] offset:256 sc0
	s_branch .LBB0_848

	.amdhsa_kernel _Z9hymba_fwd4Args
		.amdhsa_group_segment_fixed_size 0
		.amdhsa_private_segment_fixed_size 0
		.amdhsa_kernarg_size 432
		.amdhsa_user_sgpr_count 2
		.amdhsa_user_sgpr_dispatch_ptr 0
		.amdhsa_user_sgpr_queue_ptr 0
		.amdhsa_user_sgpr_kernarg_segment_ptr 1
		.amdhsa_user_sgpr_dispatch_id 0
		.amdhsa_user_sgpr_kernarg_preload_length 0
		.amdhsa_user_sgpr_kernarg_preload_offset 0
		.amdhsa_user_sgpr_private_segment_size 0
		.amdhsa_uses_dynamic_stack 0
		.amdhsa_enable_private_segment 0
		.amdhsa_system_sgpr_workgroup_id_x 1
		.amdhsa_system_sgpr_workgroup_id_y 0
		.amdhsa_system_sgpr_workgroup_id_z 0
		.amdhsa_system_sgpr_workgroup_info 0
		.amdhsa_system_vgpr_workitem_id 0
		.amdhsa_next_free_vgpr 256
		.amdhsa_next_free_sgpr 102
		.amdhsa_accum_offset 256
		.amdhsa_reserve_vcc 1
		.amdhsa_float_round_mode_32 0
		.amdhsa_float_round_mode_16_64 0
		.amdhsa_float_denorm_mode_32 3
		.amdhsa_float_denorm_mode_16_64 3
		.amdhsa_dx10_clamp 1
		.amdhsa_ieee_mode 1
		.amdhsa_fp16_overflow 0
		.amdhsa_tg_split 0
		.amdhsa_exception_fp_ieee_invalid_op 0
		.amdhsa_exception_fp_denorm_src 0
		.amdhsa_exception_fp_ieee_div_zero 0
		.amdhsa_exception_fp_ieee_overflow 0
		.amdhsa_exception_fp_ieee_underflow 0
		.amdhsa_exception_fp_ieee_inexact 0
		.amdhsa_exception_int_div_zero 0
	.end_amdhsa_kernel

amdhsa.kernels:
  - .agpr_count:     0
    .args:
      - .offset:         0
        .size:           176
        .value_kind:     by_value
      - .offset:         176
        .size:           4
        .value_kind:     hidden_block_count_x
      - .offset:         180
        .size:           4
        .value_kind:     hidden_block_count_y
      - .offset:         184
        .size:           4
        .value_kind:     hidden_block_count_z
      - .offset:         188
        .size:           2
        .value_kind:     hidden_group_size_x
      - .offset:         190
        .size:           2
        .value_kind:     hidden_group_size_y
      - .offset:         192
        .size:           2
        .value_kind:     hidden_group_size_z
      - .offset:         194
        .size:           2
        .value_kind:     hidden_remainder_x
      - .offset:         196
        .size:           2
        .value_kind:     hidden_remainder_y
      - .offset:         198
        .size:           2
        .value_kind:     hidden_remainder_z
      - .offset:         216
        .size:           8
        .value_kind:     hidden_global_offset_x
      - .offset:         224
        .size:           8
        .value_kind:     hidden_global_offset_y
      - .offset:         232
        .size:           8
        .value_kind:     hidden_global_offset_z
      - .offset:         240
        .size:           2
        .value_kind:     hidden_grid_dims
      - .offset:         296
        .size:           4
        .value_kind:     hidden_dynamic_lds_size
    .group_segment_fixed_size: 0
    .kernarg_segment_align: 8
    .kernarg_segment_size: 432
    .language:       OpenCL C
    .language_version:
      - 2
      - 0
    .max_flat_workgroup_size: 512
    .name:           _Z9hymba_fwd4Args
    .private_segment_fixed_size: 0
    .sgpr_count:     108
    .sgpr_spill_count: 133
    .symbol:         _Z9hymba_fwd4Args.kd
    .uniform_work_group_size: 1
    .uses_dynamic_stack: false
    .vgpr_count:     256
    .vgpr_spill_count: 0
    .wavefront_size: 64
